# speedup vs baseline: 1.3207x; 1.0038x over previous
.Lstep_top:
	s_and_b32 s16, s24, 1
	s_cmp_eq_u32 s16, 0
	s_cselect_b64 s[2:3], s[0:1], s[56:57]
	v_cndmask_b32_e64 v78, v79, v166, s[2:3]
	s_xor_b32 s33, s16, 1
	s_lshl_b32 s28, s33, 17
	s_add_i32 s25, s24, 1
	s_add_i32 s27, s24, 2
	s_mov_b32 s17, 0
	s_cmp_eq_u32 s24, 0
	s_cbranch_scc1 .Lpoll_issued
	s_sleep 1
	buffer_load_dwordx4 v[62:65], v78, s[8:11], s28 offen sc1
	buffer_load_dwordx4 v[66:69], v78, s[8:11], s28 offen offset:1024 sc1
	buffer_load_dwordx4 v[70:73], v78, s[8:11], s28 offen offset:2048 sc1
	buffer_load_dwordx4 v[74:77], v78, s[8:11], s28 offen offset:3072 sc1
